# QKV projection GEMMs (both layers): first K-tile of every unit peeled with C = 0 (as in GEMM1), accumulator-zeroing moves removed
# speedup vs baseline: 1.0008x; 1.0008x over previous
; #define LAS __attribute__((address_space(3)))
; #define PG8_STAGE(bufoff, gbase, voff) do { _Pragma("unroll") for (int _i = 0; _i < 2; ++_i) \
;         __builtin_amdgcn_global_load_lds((const unsigned*)((const char*)(gbase) + (voff)[_i]), (LAS unsigned*)(lds + (bufoff) + ldsw + _i * 8192), 16, 0, 0); } while (0)
; #define PG8_STAGEA(bufoff, h, ap, kb, go) do { if constexpr (GATHER) { PG8_STAGE(bufoff, (const char*)g.A + (kb), go[h]); } else { PG8_STAGE(bufoff, (ap) + (h) * hstep, voffA); } } while (0)
; #define PG8_WAIT_V(n) asm volatile("s_waitcnt vmcnt(" #n ")" ::: "memory")
; #define PG8_WAIT_L(n) asm volatile("s_waitcnt lgkmcnt(" #n ")" ::: "memory")
; #define PG8_BAR __builtin_amdgcn_s_barrier()
; template <class Epi, class Sched, bool GATHER, bool FP8 = false>
; __device__ __forceinline__ void gemm_phase(LAS unsigned char* lds, LAS int* idx, const Gemm g, const Sched& S, const Epi& E) {
;     ...
;     f32x4 acc[2][2][4][2];
; #pragma unroll
;     for (int a = 0; a < 2; ++a)
; #pragma unroll
;         for (int b = 0; b < 2; ++b)
; #pragma unroll
;             for (int m = 0; m < 4; ++m)
; #pragma unroll
;                 for (int n = 0; n < 2; ++n) acc[a][b][m][n] = (f32x4){0.f, 0.f, 0.f, 0.f};
;     bf16x8 At[4][2], B0[2][2], B1[2][2]; i32x8 At8[4], B08[2], B18[2];
;     const unsigned epi_scale = 0x01010101u * (unsigned)(127 + Epi::SEXP);
;     const unsigned one_scale = 0x7f7f7f7fu;
;     const char* cA = (const char*)g.A + (GATHER ? (size_t)0 : (size_t)cur.pm * tstep + (size_t)cur.be * g.astride);
;     const char* cB = (const char*)g.Bt + (size_t)cur.be * g.bstride + (size_t)cur.pn * tstep;
;     unsigned gc[2][2] = {{0u, 0u}, {0u, 0u}};
;     ...
;     if constexpr (GATHER) {
;         if (wid == 0) __builtin_amdgcn_global_load_lds((const unsigned*)(g.gather + (size_t)cur.pm * BM + lane * 4), (LAS unsigned*)idx, 16, 0, 0);
;         PG8_WAIT_V(0); PG8_BAR;
;         PG8_GIDX(gc, 0);
;         PG8_WAIT_L(0); PG8_BAR;
;     }
;     PG8_STAGE(PG8_SB(0, 0), cB, voffB); PG8_STAGE(PG8_SB(0, 1), cB + hstepB, voffB); PG8_STAGEA(PG8_SA(0, 0), 0, cA, 0, gc); PG8_STAGEA(PG8_SA(0, 1), 1, cA, 0, gc);
;     if (wr == 1) PG8_BAR;
;     PG8_WAIT_V(2); PG8_BAR;
;     PG8_STAGE(PG8_SB(1, 0), cB + kstep, voffB); PG8_STAGEA(PG8_SA(1, 0), 0, cA + kstep, kstep, gc); PG8_STAGE(PG8_SB(1, 1), cB + hstepB + kstep, voffB);
;     PG8_WAIT_V(6); PG8_BAR;
;     for (;;) {
.LBB0_287:
	s_cmp_lg_u32 s26, 0
	s_cselect_b64 s[26:27], -1, 0
	s_add_u32 s67, s28, 0x100
	s_mov_b32 s66, 0
	s_addc_u32 s71, s29, 0
	v_lshl_add_u64 v[210:211], s[24:25], 0, v[202:203]
	v_lshl_add_u64 v[212:213], s[24:25], 0, v[204:205]
	s_mov_b64 s[28:29], 0
	s_branch .Lpl289_289

; #define PG8_STAGE(bufoff, gbase, voff) do { _Pragma("unroll") for (int _i = 0; _i < 2; ++_i) \
;         __builtin_amdgcn_global_load_lds((const unsigned*)((const char*)(gbase) + (voff)[_i]), (LAS unsigned*)(lds + (bufoff) + ldsw + _i * 8192), 16, 0, 0); } while (0)
; #define PG8_STAGEA(bufoff, h, ap, kb, go) do { if constexpr (GATHER) { PG8_STAGE(bufoff, (const char*)g.A + (kb), go[h]); } else { PG8_STAGE(bufoff, (ap) + (h) * hstep, voffA); } } while (0)
; #define PG8_WAIT_V(n) asm volatile("s_waitcnt vmcnt(" #n ")" ::: "memory")
; #define PG8_WAIT_L(n) asm volatile("s_waitcnt lgkmcnt(" #n ")" ::: "memory")
; #define PG8_BAR __builtin_amdgcn_s_barrier()
; #define PG8_SCHED __builtin_amdgcn_sched_barrier(0)
; template <class Epi, class Sched, bool GATHER, bool FP8 = false>
; __device__ __forceinline__ void gemm_phase(LAS unsigned char* lds, LAS int* idx, const Gemm g, const Sched& S, const Epi& E) {
;     ...
;             PG8_LDB(B0, 1, 0); PG8_LDB(B1, 1, 1); PG8_SCHED; PG8_LDA(At, 1, 0); PG8_STAGEA(PG8_SA(0, 1), 1, a2, k2, g2);
;             PG8_WAIT_V(8); PG8_WAIT_L(0); PG8_BAR; PG8_MMA(0, 0, At, B0); PG8_MMA(0, 1, At, B1); PG8_BAR; PG8_SCHED;
;             PG8_LDA(At, 1, 1); PG8_STAGE(PG8_SB(1, 0), b3, voffB); PG8_STAGE(PG8_SB(1, 1), b3 + hstepB, voffB); PG8_STAGEA(PG8_SA(1, 0), 0, a3, k3, g2);
;             PG8_WAIT_V(8); PG8_WAIT_L(0); PG8_BAR; PG8_MMA(1, 0, At, B0); PG8_MMA(1, 1, At, B1); PG8_BAR; PG8_SCHED;
;             if constexpr (GATHER) { if (last) { _Pragma("unroll") for (int h = 0; h < 2; ++h) _Pragma("unroll") for (int i = 0; i < 2; ++i) gc[h][i] = g2[h][i]; } }
;             t += 2;
;         } while (t < nt);
.Lpl289_join:
	s_setprio 0
	s_barrier
	ds_read_b128 v[2:5], v235
	ds_read_b128 v[6:9], v236
	ds_read_b128 v[10:13], v237
	ds_read_b128 v[14:17], v238
	ds_read_b128 v[18:21], v239
	ds_read_b128 v[22:25], v240
	ds_read_b128 v[26:29], v241
	ds_read_b128 v[30:33], v242
	s_add_u32 s30, s30, s2
	s_addc_u32 s31, s31, s3
	s_mov_b32 m0, s49
	v_lshl_add_u64 v[246:247], s[30:31], 0, v[200:201]
	ds_read_b128 v[34:37], v244 offset:32768
	ds_read_b128 v[38:41], v244 offset:33792
	ds_read_b128 v[42:45], v244 offset:34816
	ds_read_b128 v[46:49], v244 offset:35840
	ds_read_b128 v[50:53], v244 offset:36864
	ds_read_b128 v[54:57], v244 offset:37888
	ds_read_b128 v[58:61], v244 offset:38912
	ds_read_b128 v[62:65], v244 offset:39936
	global_load_lds_dwordx4 v[246:247], off
	v_lshl_add_u64 v[246:247], s[30:31], 0, v[196:197]
	s_mov_b32 m0, s50
	s_nop 0
	global_load_lds_dwordx4 v[246:247], off
	s_waitcnt vmcnt(8)
	s_waitcnt lgkmcnt(0)
	s_barrier
	s_setprio 1
	s_waitcnt lgkmcnt(0)
	v_mfma_scale_f32_16x16x128_f8f6f4 v[190:193], v[2:9], v[34:41], v[190:193], v245, v245 op_sel_hi:[0,0,0]
	v_mfma_scale_f32_16x16x128_f8f6f4 v[186:189], v[10:17], v[34:41], v[186:189], v245, v245 op_sel_hi:[0,0,0]
	v_mfma_scale_f32_16x16x128_f8f6f4 v[174:177], v[2:9], v[42:49], v[174:177], v245, v245 op_sel_hi:[0,0,0]
	v_mfma_scale_f32_16x16x128_f8f6f4 v[170:173], v[10:17], v[42:49], v[170:173], v245, v245 op_sel_hi:[0,0,0]
	v_mfma_scale_f32_16x16x128_f8f6f4 v[158:161], v[2:9], v[50:57], v[158:161], v245, v245 op_sel_hi:[0,0,0]
	v_mfma_scale_f32_16x16x128_f8f6f4 v[154:157], v[10:17], v[50:57], v[154:157], v245, v245 op_sel_hi:[0,0,0]
	v_mfma_scale_f32_16x16x128_f8f6f4 v[142:145], v[2:9], v[58:65], v[142:145], v245, v245 op_sel_hi:[0,0,0]
	v_mfma_scale_f32_16x16x128_f8f6f4 v[138:141], v[10:17], v[58:65], v[138:141], v245, v245 op_sel_hi:[0,0,0]
	s_setprio 0
	s_setprio 1
	v_mfma_scale_f32_16x16x128_f8f6f4 v[182:185], v[18:25], v[34:41], v[182:185], v245, v245 op_sel_hi:[0,0,0]
	v_mfma_scale_f32_16x16x128_f8f6f4 v[178:181], v[26:33], v[34:41], v[178:181], v245, v245 op_sel_hi:[0,0,0]
	v_mfma_scale_f32_16x16x128_f8f6f4 v[166:169], v[18:25], v[42:49], v[166:169], v245, v245 op_sel_hi:[0,0,0]
	v_mfma_scale_f32_16x16x128_f8f6f4 v[162:165], v[26:33], v[42:49], v[162:165], v245, v245 op_sel_hi:[0,0,0]
	v_mfma_scale_f32_16x16x128_f8f6f4 v[150:153], v[18:25], v[50:57], v[150:153], v245, v245 op_sel_hi:[0,0,0]
	v_mfma_scale_f32_16x16x128_f8f6f4 v[146:149], v[26:33], v[50:57], v[146:149], v245, v245 op_sel_hi:[0,0,0]
	v_mfma_scale_f32_16x16x128_f8f6f4 v[134:137], v[18:25], v[58:65], v[134:137], v245, v245 op_sel_hi:[0,0,0]
	v_mfma_scale_f32_16x16x128_f8f6f4 v[130:133], v[26:33], v[58:65], v[130:133], v245, v245 op_sel_hi:[0,0,0]
	s_setprio 0
	s_barrier
	s_mov_b32 m0, s51
	v_lshl_add_u64 v[214:215], v[214:215], 0, s[14:15]
	ds_read_b128 v[34:37], v244 offset:49152
	ds_read_b128 v[38:41], v244 offset:50176
	ds_read_b128 v[42:45], v244 offset:51200
	ds_read_b128 v[46:49], v244 offset:52224
	ds_read_b128 v[50:53], v244 offset:53248
	ds_read_b128 v[54:57], v244 offset:54272
	ds_read_b128 v[58:61], v244 offset:55296
	ds_read_b128 v[62:65], v244 offset:56320
	global_load_lds_dwordx4 v[214:215], off
	v_lshl_add_u64 v[214:215], v[216:217], 0, s[14:15]
	s_mov_b32 m0, s52
	s_nop 0
	global_load_lds_dwordx4 v[214:215], off
	v_lshl_add_u64 v[214:215], v[218:219], 0, s[14:15]
	s_mov_b32 m0, s55
	s_nop 0
	global_load_lds_dwordx4 v[214:215], off
	v_lshl_add_u64 v[214:215], v[220:221], 0, s[14:15]
	s_mov_b32 m0, s56
	s_nop 0
	global_load_lds_dwordx4 v[214:215], off
	v_lshl_add_u64 v[214:215], v[222:223], 0, s[14:15]
	s_mov_b32 m0, s53
	s_nop 0
	global_load_lds_dwordx4 v[214:215], off
	v_lshl_add_u64 v[214:215], v[224:225], 0, s[14:15]
	s_mov_b32 m0, s54
	s_nop 0
	global_load_lds_dwordx4 v[214:215], off
	s_waitcnt vmcnt(8)
	s_waitcnt lgkmcnt(0)
	s_barrier
	s_setprio 1
	s_waitcnt lgkmcnt(0)
	v_mfma_scale_f32_16x16x128_f8f6f4 v[126:129], v[2:9], v[34:41], v[126:129], v245, v245 op_sel_hi:[0,0,0]
	v_mfma_scale_f32_16x16x128_f8f6f4 v[122:125], v[10:17], v[34:41], v[122:125], v245, v245 op_sel_hi:[0,0,0]
	v_mfma_scale_f32_16x16x128_f8f6f4 v[110:113], v[2:9], v[42:49], v[110:113], v245, v245 op_sel_hi:[0,0,0]
	v_mfma_scale_f32_16x16x128_f8f6f4 v[106:109], v[10:17], v[42:49], v[106:109], v245, v245 op_sel_hi:[0,0,0]
	v_mfma_scale_f32_16x16x128_f8f6f4 v[94:97], v[2:9], v[50:57], v[94:97], v245, v245 op_sel_hi:[0,0,0]
	v_mfma_scale_f32_16x16x128_f8f6f4 v[90:93], v[10:17], v[50:57], v[90:93], v245, v245 op_sel_hi:[0,0,0]
	v_mfma_scale_f32_16x16x128_f8f6f4 v[78:81], v[2:9], v[58:65], v[78:81], v245, v245 op_sel_hi:[0,0,0]
	v_mfma_scale_f32_16x16x128_f8f6f4 v[74:77], v[10:17], v[58:65], v[74:77], v245, v245 op_sel_hi:[0,0,0]
	s_setprio 0
	s_setprio 1
	v_mfma_scale_f32_16x16x128_f8f6f4 v[118:121], v[18:25], v[34:41], v[118:121], v245, v245 op_sel_hi:[0,0,0]
	v_mfma_scale_f32_16x16x128_f8f6f4 v[114:117], v[26:33], v[34:41], v[114:117], v245, v245 op_sel_hi:[0,0,0]
	v_mfma_scale_f32_16x16x128_f8f6f4 v[102:105], v[18:25], v[42:49], v[102:105], v245, v245 op_sel_hi:[0,0,0]
	v_mfma_scale_f32_16x16x128_f8f6f4 v[98:101], v[26:33], v[42:49], v[98:101], v245, v245 op_sel_hi:[0,0,0]
	v_mfma_scale_f32_16x16x128_f8f6f4 v[86:89], v[18:25], v[50:57], v[86:89], v245, v245 op_sel_hi:[0,0,0]
	v_mfma_scale_f32_16x16x128_f8f6f4 v[82:85], v[26:33], v[50:57], v[82:85], v245, v245 op_sel_hi:[0,0,0]
	v_mfma_scale_f32_16x16x128_f8f6f4 v[70:73], v[18:25], v[58:65], v[70:73], v245, v245 op_sel_hi:[0,0,0]
	v_mfma_scale_f32_16x16x128_f8f6f4 v[66:69], v[26:33], v[58:65], v[66:69], v245, v245 op_sel_hi:[0,0,0]
	s_setprio 0
	s_barrier
	s_add_u32 s28, s28, 0x100
	s_addc_u32 s29, s29, 0
	s_cmp_lt_i32 s66, s57
	s_cbranch_scc0 .LBB0_297

; #define PG8_STAGEA(bufoff, h, ap, kb, go) do { if constexpr (GATHER) { PG8_STAGE(bufoff, (const char*)g.A + (kb), go[h]); } else { PG8_STAGE(bufoff, (ap) + (h) * hstep, voffA); } } while (0)
; #define PG8_WAIT_L(n) asm volatile("s_waitcnt lgkmcnt(" #n ")" ::: "memory")
; #define PG8_WAIT_V8R() do { if (relax) { if (GATHER && wid == 0 && has_next) asm volatile("s_waitcnt vmcnt(%0)" :: "n"(9 + Epi::NSTORES) : "memory"); else asm volatile("s_waitcnt vmcnt(%0)" :: "n"(8 + Epi::NSTORES) : "memory"); } else PG8_WAIT_V(8); } while (0)
; #define PG8_BAR __builtin_amdgcn_s_barrier()
; #define PG8_SCHED __builtin_amdgcn_sched_barrier(0)
; template <class Epi, class Sched, bool GATHER, bool FP8 = false>
; __device__ __forceinline__ void gemm_phase(LAS unsigned char* lds, LAS int* idx, const Gemm g, const Sched& S, const Epi& E) {
;     ...
;             const int relax = __builtin_amdgcn_readfirstlane(((t == 0) && (ui > 0)) ? 1 : 0);
;             PG8_LDB(B0, 0, 0); PG8_LDB(B1, 0, 1); PG8_SCHED; PG8_LDA(At, 0, 0); PG8_STAGEA(PG8_SA(1, 1), 1, a1, k1, gc);
;             PG8_WAIT_V8R(); PG8_WAIT_L(0); PG8_BAR; PG8_MMA(0, 0, At, B0); PG8_MMA(0, 1, At, B1); PG8_BAR; PG8_SCHED;
.LBB0_295:
	s_andn2_b64 vcc, exec, s[36:37]
	s_cbranch_vccnz .LBB0_288
	s_waitcnt vmcnt(24)
	s_branch .LBB0_288
.Lpl289_289:
	ds_read_b128 v[26:29], v226
	ds_read_b128 v[30:33], v227
	ds_read_b128 v[18:21], v228
	ds_read_b128 v[22:25], v229
	ds_read_b128 v[10:13], v231
	ds_read_b128 v[14:17], v232
	ds_read_b128 v[2:5], v233
	ds_read_b128 v[6:9], v234
	s_cmp_eq_u32 s66, 0
	s_cselect_b64 s[30:31], -1, 0
	s_and_b64 s[30:31], s[26:27], s[30:31]
	v_lshl_add_u64 v[214:215], v[210:211], 0, s[28:29]
	s_add_i32 m0, s43, 0xc000
	ds_read_b128 v[58:61], v244
	ds_read_b128 v[62:65], v244 offset:1024
	ds_read_b128 v[50:53], v244 offset:2048
	ds_read_b128 v[54:57], v244 offset:3072
	ds_read_b128 v[42:45], v244 offset:4096
	ds_read_b128 v[46:49], v244 offset:5120
	ds_read_b128 v[34:37], v244 offset:6144
	ds_read_b128 v[38:41], v244 offset:7168
	global_load_lds_dwordx4 v[214:215], off
	v_lshl_add_u64 v[214:215], v[212:213], 0, s[28:29]
	s_add_i32 m0, s43, 0xe000
	s_nop 0
	global_load_lds_dwordx4 v[214:215], off
	s_and_b64 vcc, exec, s[30:31]
	s_not_b64 s[34:35], s[30:31]
	s_mov_b64 s[30:31], -1
	s_cbranch_vccnz .Lpl289_291
	s_waitcnt vmcnt(8)
	s_mov_b64 s[30:31], 0

; #define PG8_STAGE(bufoff, gbase, voff) do { _Pragma("unroll") for (int _i = 0; _i < 2; ++_i) \
;         __builtin_amdgcn_global_load_lds((const unsigned*)((const char*)(gbase) + (voff)[_i]), (LAS unsigned*)(lds + (bufoff) + ldsw + _i * 8192), 16, 0, 0); } while (0)
; #define PG8_STAGEA(bufoff, h, ap, kb, go) do { if constexpr (GATHER) { PG8_STAGE(bufoff, (const char*)g.A + (kb), go[h]); } else { PG8_STAGE(bufoff, (ap) + (h) * hstep, voffA); } } while (0)
; #define PG8_WAIT_L(n) asm volatile("s_waitcnt lgkmcnt(" #n ")" ::: "memory")
; #define PG8_WAIT_V8R() do { if (relax) { if (GATHER && wid == 0 && has_next) asm volatile("s_waitcnt vmcnt(%0)" :: "n"(9 + Epi::NSTORES) : "memory"); else asm volatile("s_waitcnt vmcnt(%0)" :: "n"(8 + Epi::NSTORES) : "memory"); } else PG8_WAIT_V(8); } while (0)
; #define PG8_BAR __builtin_amdgcn_s_barrier()
; template <class Epi, class Sched, bool GATHER, bool FP8 = false>
; __device__ __forceinline__ void gemm_phase(LAS unsigned char* lds, LAS int* idx, const Gemm g, const Sched& S, const Epi& E) {
;     ...
;             const bool last = (t == nt - 2);
;             const char* a1 = cA + (size_t)(t + 1) * kstep;
;             const char* a2 = last ? nA : cA + (size_t)(t + 2) * kstep; const char* b2 = last ? nB : cB + (size_t)(t + 2) * kstep;
;             const char* a3 = a2 + kstep; const char* b3 = b2 + kstep;
;             const size_t k1 = (size_t)(t + 1) * kstep, k2 = last ? (size_t)0 : (size_t)(t + 2) * kstep, k3 = k2 + kstep;
;             unsigned g2[2][2];
; #pragma unroll
;             for (int h = 0; h < 2; ++h)
; #pragma unroll
;                 for (int i = 0; i < 2; ++i) g2[h][i] = gc[h][i];
;             if constexpr (GATHER) { if (last && has_next) PG8_GIDX(g2, ((ui + 1) & 1) * BM); }
;             const int relax = __builtin_amdgcn_readfirstlane(((t == 0) && (ui > 0)) ? 1 : 0);
;             PG8_LDB(B0, 0, 0); PG8_LDB(B1, 0, 1); PG8_SCHED; PG8_LDA(At, 0, 0); PG8_STAGEA(PG8_SA(1, 1), 1, a1, k1, gc);
;             PG8_WAIT_V8R(); PG8_WAIT_L(0); PG8_BAR; PG8_MMA(0, 0, At, B0); PG8_MMA(0, 1, At, B1); PG8_BAR; PG8_SCHED;
;             PG8_LDA(At, 0, 1); PG8_STAGE(PG8_SB(0, 0), b2, voffB); PG8_STAGE(PG8_SB(0, 1), b2 + hstepB, voffB); PG8_STAGEA(PG8_SA(0, 0), 0, a2, k2, g2);
;             PG8_WAIT_V8R(); PG8_WAIT_L(0); PG8_BAR; PG8_MMA(1, 0, At, B0); PG8_MMA(1, 1, At, B1); PG8_BAR; PG8_SCHED;
.Lpl289_293:
	s_add_u32 s30, s24, s28
	s_addc_u32 s31, s25, s29
	s_add_u32 s30, s30, 0x100
	s_addc_u32 s31, s31, 0
	s_add_u32 s36, s67, s28
	s_addc_u32 s37, s71, s29
	s_waitcnt lgkmcnt(0)
	s_cmp_eq_u32 s58, s66
	s_cselect_b32 s31, s9, s31
	s_cselect_b32 s30, s8, s30
	s_cselect_b32 s37, s23, s37
	s_cselect_b32 s36, s22, s36
	s_barrier
	s_setprio 1
	s_waitcnt lgkmcnt(0)
	v_mfma_scale_f32_16x16x128_f8f6f4 v[190:193], v[26:33], v[58:65], 0, v245, v245 op_sel_hi:[0,0,0]
	v_mfma_scale_f32_16x16x128_f8f6f4 v[186:189], v[18:25], v[58:65], 0, v245, v245 op_sel_hi:[0,0,0]
	v_mfma_scale_f32_16x16x128_f8f6f4 v[174:177], v[26:33], v[50:57], 0, v245, v245 op_sel_hi:[0,0,0]
	v_mfma_scale_f32_16x16x128_f8f6f4 v[170:173], v[18:25], v[50:57], 0, v245, v245 op_sel_hi:[0,0,0]
	v_mfma_scale_f32_16x16x128_f8f6f4 v[158:161], v[26:33], v[42:49], 0, v245, v245 op_sel_hi:[0,0,0]
	v_mfma_scale_f32_16x16x128_f8f6f4 v[154:157], v[18:25], v[42:49], 0, v245, v245 op_sel_hi:[0,0,0]
	v_mfma_scale_f32_16x16x128_f8f6f4 v[142:145], v[26:33], v[34:41], 0, v245, v245 op_sel_hi:[0,0,0]
	v_mfma_scale_f32_16x16x128_f8f6f4 v[138:141], v[18:25], v[34:41], 0, v245, v245 op_sel_hi:[0,0,0]
	s_setprio 0
	s_setprio 1
	v_mfma_scale_f32_16x16x128_f8f6f4 v[182:185], v[10:17], v[58:65], 0, v245, v245 op_sel_hi:[0,0,0]
	v_mfma_scale_f32_16x16x128_f8f6f4 v[178:181], v[2:9], v[58:65], 0, v245, v245 op_sel_hi:[0,0,0]
	v_mfma_scale_f32_16x16x128_f8f6f4 v[166:169], v[10:17], v[50:57], 0, v245, v245 op_sel_hi:[0,0,0]
	v_mfma_scale_f32_16x16x128_f8f6f4 v[162:165], v[2:9], v[50:57], 0, v245, v245 op_sel_hi:[0,0,0]
	v_mfma_scale_f32_16x16x128_f8f6f4 v[150:153], v[10:17], v[42:49], 0, v245, v245 op_sel_hi:[0,0,0]
	v_mfma_scale_f32_16x16x128_f8f6f4 v[146:149], v[2:9], v[42:49], 0, v245, v245 op_sel_hi:[0,0,0]
	v_mfma_scale_f32_16x16x128_f8f6f4 v[134:137], v[10:17], v[34:41], 0, v245, v245 op_sel_hi:[0,0,0]
	v_mfma_scale_f32_16x16x128_f8f6f4 v[130:133], v[2:9], v[34:41], 0, v245, v245 op_sel_hi:[0,0,0]
	s_setprio 0
	s_barrier
	s_mov_b32 m0, s44
	v_lshl_add_u64 v[214:215], s[36:37], 0, v[198:199]
	v_lshl_add_u64 v[216:217], s[36:37], 0, v[194:195]
	s_add_u32 s36, s36, s10
	ds_read_b128 v[58:61], v244 offset:16384
	ds_read_b128 v[62:65], v244 offset:17408
	ds_read_b128 v[50:53], v244 offset:18432
	ds_read_b128 v[54:57], v244 offset:19456
	ds_read_b128 v[42:45], v244 offset:20480
	ds_read_b128 v[46:49], v244 offset:21504
	ds_read_b128 v[34:37], v244 offset:22528
	ds_read_b128 v[38:41], v244 offset:23552
	global_load_lds_dwordx4 v[214:215], off
	s_mov_b32 m0, s45
	s_addc_u32 s37, s37, s11
	global_load_lds_dwordx4 v[216:217], off
	v_lshl_add_u64 v[218:219], s[36:37], 0, v[198:199]
	s_mov_b32 m0, s46
	v_lshl_add_u64 v[220:221], s[36:37], 0, v[194:195]
	global_load_lds_dwordx4 v[218:219], off
	s_mov_b32 m0, s47
	v_lshl_add_u64 v[222:223], s[30:31], 0, v[200:201]
	global_load_lds_dwordx4 v[220:221], off
	s_mov_b32 m0, s43
	v_lshl_add_u64 v[224:225], s[30:31], 0, v[196:197]
	global_load_lds_dwordx4 v[222:223], off
	s_mov_b32 m0, s48
	s_mov_b64 s[36:37], -1
	global_load_lds_dwordx4 v[224:225], off
	s_and_b64 vcc, exec, s[34:35]
	s_cbranch_vccz .Lpl289_295
	s_waitcnt vmcnt(8)
	s_mov_b64 s[36:37], 0

; #define PG8_STAGE(bufoff, gbase, voff) do { _Pragma("unroll") for (int _i = 0; _i < 2; ++_i) \
;         __builtin_amdgcn_global_load_lds((const unsigned*)((const char*)(gbase) + (voff)[_i]), (LAS unsigned*)(lds + (bufoff) + ldsw + _i * 8192), 16, 0, 0); } while (0)
; #define PG8_STAGEA(bufoff, h, ap, kb, go) do { if constexpr (GATHER) { PG8_STAGE(bufoff, (const char*)g.A + (kb), go[h]); } else { PG8_STAGE(bufoff, (ap) + (h) * hstep, voffA); } } while (0)
; #define PG8_WAIT_V(n) asm volatile("s_waitcnt vmcnt(" #n ")" ::: "memory")
; #define PG8_WAIT_L(n) asm volatile("s_waitcnt lgkmcnt(" #n ")" ::: "memory")
; #define PG8_WAIT_V8R() do { if (relax) { if (GATHER && wid == 0 && has_next) asm volatile("s_waitcnt vmcnt(%0)" :: "n"(9 + Epi::NSTORES) : "memory"); else asm volatile("s_waitcnt vmcnt(%0)" :: "n"(8 + Epi::NSTORES) : "memory"); } else PG8_WAIT_V(8); } while (0)
; #define PG8_BAR __builtin_amdgcn_s_barrier()
; #define PG8_SCHED __builtin_amdgcn_sched_barrier(0)
; template <class Epi, class Sched, bool GATHER, bool FP8 = false>
; __device__ __forceinline__ void gemm_phase(LAS unsigned char* lds, LAS int* idx, const Gemm g, const Sched& S, const Epi& E) {
;     ...
;             PG8_WAIT_V8R(); PG8_WAIT_L(0); PG8_BAR; PG8_MMA(1, 0, At, B0); PG8_MMA(1, 1, At, B1); PG8_BAR; PG8_SCHED;
;             PG8_LDB(B0, 1, 0); PG8_LDB(B1, 1, 1); PG8_SCHED; PG8_LDA(At, 1, 0); PG8_STAGEA(PG8_SA(0, 1), 1, a2, k2, g2);
;             PG8_WAIT_V(8); PG8_WAIT_L(0); PG8_BAR; PG8_MMA(0, 0, At, B0); PG8_MMA(0, 1, At, B1); PG8_BAR; PG8_SCHED;
;             PG8_LDA(At, 1, 1); PG8_STAGE(PG8_SB(1, 0), b3, voffB); PG8_STAGE(PG8_SB(1, 1), b3 + hstepB, voffB); PG8_STAGEA(PG8_SA(1, 0), 0, a3, k3, g2);
;             PG8_WAIT_V(8); PG8_WAIT_L(0); PG8_BAR; PG8_MMA(1, 0, At, B0); PG8_MMA(1, 1, At, B1); PG8_BAR; PG8_SCHED;
;             if constexpr (GATHER) { if (last) { _Pragma("unroll") for (int h = 0; h < 2; ++h) _Pragma("unroll") for (int i = 0; i < 2; ++i) gc[h][i] = g2[h][i]; } }
;             t += 2;
.Lpl289_288:
	s_waitcnt lgkmcnt(0)
	s_add_i32 s66, s66, 2
	s_barrier
	s_setprio 1
	s_waitcnt lgkmcnt(0)
	v_mfma_scale_f32_16x16x128_f8f6f4 v[126:129], v[26:33], v[58:65], 0, v245, v245 op_sel_hi:[0,0,0]
	v_mfma_scale_f32_16x16x128_f8f6f4 v[122:125], v[18:25], v[58:65], 0, v245, v245 op_sel_hi:[0,0,0]
	v_mfma_scale_f32_16x16x128_f8f6f4 v[110:113], v[26:33], v[50:57], 0, v245, v245 op_sel_hi:[0,0,0]
	v_mfma_scale_f32_16x16x128_f8f6f4 v[106:109], v[18:25], v[50:57], 0, v245, v245 op_sel_hi:[0,0,0]
	v_mfma_scale_f32_16x16x128_f8f6f4 v[94:97], v[26:33], v[42:49], 0, v245, v245 op_sel_hi:[0,0,0]
	v_mfma_scale_f32_16x16x128_f8f6f4 v[90:93], v[18:25], v[42:49], 0, v245, v245 op_sel_hi:[0,0,0]
	v_mfma_scale_f32_16x16x128_f8f6f4 v[78:81], v[26:33], v[34:41], 0, v245, v245 op_sel_hi:[0,0,0]
	v_mfma_scale_f32_16x16x128_f8f6f4 v[74:77], v[18:25], v[34:41], 0, v245, v245 op_sel_hi:[0,0,0]
	s_setprio 0
	s_setprio 1
	v_mfma_scale_f32_16x16x128_f8f6f4 v[118:121], v[10:17], v[58:65], 0, v245, v245 op_sel_hi:[0,0,0]
	v_mfma_scale_f32_16x16x128_f8f6f4 v[114:117], v[2:9], v[58:65], 0, v245, v245 op_sel_hi:[0,0,0]
	v_mfma_scale_f32_16x16x128_f8f6f4 v[102:105], v[10:17], v[50:57], 0, v245, v245 op_sel_hi:[0,0,0]
	v_mfma_scale_f32_16x16x128_f8f6f4 v[98:101], v[2:9], v[50:57], 0, v245, v245 op_sel_hi:[0,0,0]
	v_mfma_scale_f32_16x16x128_f8f6f4 v[86:89], v[10:17], v[42:49], 0, v245, v245 op_sel_hi:[0,0,0]
	v_mfma_scale_f32_16x16x128_f8f6f4 v[82:85], v[2:9], v[42:49], 0, v245, v245 op_sel_hi:[0,0,0]
	v_mfma_scale_f32_16x16x128_f8f6f4 v[70:73], v[10:17], v[34:41], 0, v245, v245 op_sel_hi:[0,0,0]
	v_mfma_scale_f32_16x16x128_f8f6f4 v[66:69], v[2:9], v[34:41], 0, v245, v245 op_sel_hi:[0,0,0]
	s_branch .Lpl289_join

; #define LAS __attribute__((address_space(3)))
; #define PG8_STAGE(bufoff, gbase, voff) do { _Pragma("unroll") for (int _i = 0; _i < 2; ++_i) \
;         __builtin_amdgcn_global_load_lds((const unsigned*)((const char*)(gbase) + (voff)[_i]), (LAS unsigned*)(lds + (bufoff) + ldsw + _i * 8192), 16, 0, 0); } while (0)
; #define PG8_STAGEA(bufoff, h, ap, kb, go) do { if constexpr (GATHER) { PG8_STAGE(bufoff, (const char*)g.A + (kb), go[h]); } else { PG8_STAGE(bufoff, (ap) + (h) * hstep, voffA); } } while (0)
; #define PG8_WAIT_V(n) asm volatile("s_waitcnt vmcnt(" #n ")" ::: "memory")
; #define PG8_WAIT_L(n) asm volatile("s_waitcnt lgkmcnt(" #n ")" ::: "memory")
; #define PG8_BAR __builtin_amdgcn_s_barrier()
; template <class Epi, class Sched, bool GATHER, bool FP8 = false>
; __device__ __forceinline__ void gemm_phase(LAS unsigned char* lds, LAS int* idx, const Gemm g, const Sched& S, const Epi& E) {
;     ...
;     f32x4 acc[2][2][4][2];
; #pragma unroll
;     for (int a = 0; a < 2; ++a)
; #pragma unroll
;         for (int b = 0; b < 2; ++b)
; #pragma unroll
;             for (int m = 0; m < 4; ++m)
; #pragma unroll
;                 for (int n = 0; n < 2; ++n) acc[a][b][m][n] = (f32x4){0.f, 0.f, 0.f, 0.f};
;     bf16x8 At[4][2], B0[2][2], B1[2][2]; i32x8 At8[4], B08[2], B18[2];
;     const unsigned epi_scale = 0x01010101u * (unsigned)(127 + Epi::SEXP);
;     const unsigned one_scale = 0x7f7f7f7fu;
;     const char* cA = (const char*)g.A + (GATHER ? (size_t)0 : (size_t)cur.pm * tstep + (size_t)cur.be * g.astride);
;     const char* cB = (const char*)g.Bt + (size_t)cur.be * g.bstride + (size_t)cur.pn * tstep;
;     unsigned gc[2][2] = {{0u, 0u}, {0u, 0u}};
;     ...
;     if constexpr (GATHER) {
;         if (wid == 0) __builtin_amdgcn_global_load_lds((const unsigned*)(g.gather + (size_t)cur.pm * BM + lane * 4), (LAS unsigned*)idx, 16, 0, 0);
;         PG8_WAIT_V(0); PG8_BAR;
;         PG8_GIDX(gc, 0);
;         PG8_WAIT_L(0); PG8_BAR;
;     }
;     PG8_STAGE(PG8_SB(0, 0), cB, voffB); PG8_STAGE(PG8_SB(0, 1), cB + hstepB, voffB); PG8_STAGEA(PG8_SA(0, 0), 0, cA, 0, gc); PG8_STAGEA(PG8_SA(0, 1), 1, cA, 0, gc);
;     if (wr == 1) PG8_BAR;
;     PG8_WAIT_V(2); PG8_BAR;
;     PG8_STAGE(PG8_SB(1, 0), cB + kstep, voffB); PG8_STAGEA(PG8_SA(1, 0), 0, cA + kstep, kstep, gc); PG8_STAGE(PG8_SB(1, 1), cB + hstepB + kstep, voffB);
;     PG8_WAIT_V(6); PG8_BAR;
;     for (;;) {
.LBB0_1012:
	s_cmp_lg_u32 s26, 0
	s_cselect_b64 s[8:9], -1, 0
	s_add_u32 s69, s24, 0x100
	s_mov_b32 s68, 0
	s_addc_u32 s70, s25, 0
	v_lshl_add_u64 v[212:213], s[22:23], 0, v[204:205]
	v_lshl_add_u64 v[214:215], s[22:23], 0, v[206:207]
	s_mov_b64 s[24:25], 0
	s_branch .Lpl1014_1014

; #define PG8_STAGE(bufoff, gbase, voff) do { _Pragma("unroll") for (int _i = 0; _i < 2; ++_i) \
;         __builtin_amdgcn_global_load_lds((const unsigned*)((const char*)(gbase) + (voff)[_i]), (LAS unsigned*)(lds + (bufoff) + ldsw + _i * 8192), 16, 0, 0); } while (0)
; #define PG8_STAGEA(bufoff, h, ap, kb, go) do { if constexpr (GATHER) { PG8_STAGE(bufoff, (const char*)g.A + (kb), go[h]); } else { PG8_STAGE(bufoff, (ap) + (h) * hstep, voffA); } } while (0)
; #define PG8_WAIT_V(n) asm volatile("s_waitcnt vmcnt(" #n ")" ::: "memory")
; #define PG8_WAIT_L(n) asm volatile("s_waitcnt lgkmcnt(" #n ")" ::: "memory")
; #define PG8_BAR __builtin_amdgcn_s_barrier()
; #define PG8_SCHED __builtin_amdgcn_sched_barrier(0)
; template <class Epi, class Sched, bool GATHER, bool FP8 = false>
; __device__ __forceinline__ void gemm_phase(LAS unsigned char* lds, LAS int* idx, const Gemm g, const Sched& S, const Epi& E) {
;     ...
;             PG8_LDB(B0, 1, 0); PG8_LDB(B1, 1, 1); PG8_SCHED; PG8_LDA(At, 1, 0); PG8_STAGEA(PG8_SA(0, 1), 1, a2, k2, g2);
;             PG8_WAIT_V(8); PG8_WAIT_L(0); PG8_BAR; PG8_MMA(0, 0, At, B0); PG8_MMA(0, 1, At, B1); PG8_BAR; PG8_SCHED;
;             PG8_LDA(At, 1, 1); PG8_STAGE(PG8_SB(1, 0), b3, voffB); PG8_STAGE(PG8_SB(1, 1), b3 + hstepB, voffB); PG8_STAGEA(PG8_SA(1, 0), 0, a3, k3, g2);
;             PG8_WAIT_V(8); PG8_WAIT_L(0); PG8_BAR; PG8_MMA(1, 0, At, B0); PG8_MMA(1, 1, At, B1); PG8_BAR; PG8_SCHED;
;             if constexpr (GATHER) { if (last) { _Pragma("unroll") for (int h = 0; h < 2; ++h) _Pragma("unroll") for (int i = 0; i < 2; ++i) gc[h][i] = g2[h][i]; } }
;             t += 2;
;         } while (t < nt);
.Lpl1014_join:
	s_setprio 0
	s_barrier
	ds_read_b128 v[2:5], v238
	ds_read_b128 v[6:9], v239
	ds_read_b128 v[10:13], v240
	ds_read_b128 v[14:17], v241
	ds_read_b128 v[18:21], v242
	ds_read_b128 v[22:25], v243
	ds_read_b128 v[26:29], v244
	ds_read_b128 v[30:33], v245
	s_add_u32 s26, s26, s2
	s_addc_u32 s27, s27, s3
	s_mov_b32 m0, s44
	v_lshl_add_u64 v[252:253], s[26:27], 0, v[194:195]
	ds_read_b128 v[34:37], v247 offset:32768
	ds_read_b128 v[38:41], v247 offset:33792
	ds_read_b128 v[42:45], v247 offset:34816
	ds_read_b128 v[46:49], v247 offset:35840
	ds_read_b128 v[50:53], v247 offset:36864
	ds_read_b128 v[54:57], v247 offset:37888
	ds_read_b128 v[58:61], v247 offset:38912
	ds_read_b128 v[62:65], v247 offset:39936
	global_load_lds_dwordx4 v[252:253], off
	v_lshl_add_u64 v[252:253], s[26:27], 0, v[198:199]
	s_mov_b32 m0, s45
	s_nop 0
	global_load_lds_dwordx4 v[252:253], off
	s_waitcnt vmcnt(8)
	s_waitcnt lgkmcnt(0)
	s_barrier
	s_setprio 1
	s_waitcnt lgkmcnt(0)
	v_mfma_scale_f32_16x16x128_f8f6f4 v[190:193], v[2:9], v[34:41], v[190:193], v248, v248 op_sel_hi:[0,0,0]
	v_mfma_scale_f32_16x16x128_f8f6f4 v[186:189], v[10:17], v[34:41], v[186:189], v248, v248 op_sel_hi:[0,0,0]
	v_mfma_scale_f32_16x16x128_f8f6f4 v[174:177], v[2:9], v[42:49], v[174:177], v248, v248 op_sel_hi:[0,0,0]
	v_mfma_scale_f32_16x16x128_f8f6f4 v[170:173], v[10:17], v[42:49], v[170:173], v248, v248 op_sel_hi:[0,0,0]
	v_mfma_scale_f32_16x16x128_f8f6f4 v[158:161], v[2:9], v[50:57], v[158:161], v248, v248 op_sel_hi:[0,0,0]
	v_mfma_scale_f32_16x16x128_f8f6f4 v[154:157], v[10:17], v[50:57], v[154:157], v248, v248 op_sel_hi:[0,0,0]
	v_mfma_scale_f32_16x16x128_f8f6f4 v[142:145], v[2:9], v[58:65], v[142:145], v248, v248 op_sel_hi:[0,0,0]
	v_mfma_scale_f32_16x16x128_f8f6f4 v[138:141], v[10:17], v[58:65], v[138:141], v248, v248 op_sel_hi:[0,0,0]
	s_setprio 0
	s_setprio 1
	v_mfma_scale_f32_16x16x128_f8f6f4 v[182:185], v[18:25], v[34:41], v[182:185], v248, v248 op_sel_hi:[0,0,0]
	v_mfma_scale_f32_16x16x128_f8f6f4 v[178:181], v[26:33], v[34:41], v[178:181], v248, v248 op_sel_hi:[0,0,0]
	v_mfma_scale_f32_16x16x128_f8f6f4 v[166:169], v[18:25], v[42:49], v[166:169], v248, v248 op_sel_hi:[0,0,0]
	v_mfma_scale_f32_16x16x128_f8f6f4 v[162:165], v[26:33], v[42:49], v[162:165], v248, v248 op_sel_hi:[0,0,0]
	v_mfma_scale_f32_16x16x128_f8f6f4 v[150:153], v[18:25], v[50:57], v[150:153], v248, v248 op_sel_hi:[0,0,0]
	v_mfma_scale_f32_16x16x128_f8f6f4 v[146:149], v[26:33], v[50:57], v[146:149], v248, v248 op_sel_hi:[0,0,0]
	v_mfma_scale_f32_16x16x128_f8f6f4 v[134:137], v[18:25], v[58:65], v[134:137], v248, v248 op_sel_hi:[0,0,0]
	v_mfma_scale_f32_16x16x128_f8f6f4 v[130:133], v[26:33], v[58:65], v[130:133], v248, v248 op_sel_hi:[0,0,0]
	s_setprio 0
	s_barrier
	s_mov_b32 m0, s46
	v_lshl_add_u64 v[216:217], v[216:217], 0, s[14:15]
	ds_read_b128 v[34:37], v247 offset:49152
	ds_read_b128 v[38:41], v247 offset:50176
	ds_read_b128 v[42:45], v247 offset:51200
	ds_read_b128 v[46:49], v247 offset:52224
	ds_read_b128 v[50:53], v247 offset:53248
	ds_read_b128 v[54:57], v247 offset:54272
	ds_read_b128 v[58:61], v247 offset:55296
	ds_read_b128 v[62:65], v247 offset:56320
	global_load_lds_dwordx4 v[216:217], off
	v_lshl_add_u64 v[216:217], v[218:219], 0, s[14:15]
	s_mov_b32 m0, s47
	s_nop 0
	global_load_lds_dwordx4 v[216:217], off
	v_lshl_add_u64 v[216:217], v[220:221], 0, s[14:15]
	s_mov_b32 m0, s50
	s_nop 0
	global_load_lds_dwordx4 v[216:217], off
	v_lshl_add_u64 v[216:217], v[222:223], 0, s[14:15]
	s_mov_b32 m0, s51
	s_nop 0
	global_load_lds_dwordx4 v[216:217], off
	v_lshl_add_u64 v[216:217], v[224:225], 0, s[14:15]
	s_mov_b32 m0, s48
	s_nop 0
	global_load_lds_dwordx4 v[216:217], off
	v_lshl_add_u64 v[216:217], v[226:227], 0, s[14:15]
	s_mov_b32 m0, s49
	s_nop 0
	global_load_lds_dwordx4 v[216:217], off
	s_waitcnt vmcnt(8)
	s_waitcnt lgkmcnt(0)
	s_barrier
	s_setprio 1
	s_waitcnt lgkmcnt(0)
	v_mfma_scale_f32_16x16x128_f8f6f4 v[126:129], v[2:9], v[34:41], v[126:129], v248, v248 op_sel_hi:[0,0,0]
	v_mfma_scale_f32_16x16x128_f8f6f4 v[122:125], v[10:17], v[34:41], v[122:125], v248, v248 op_sel_hi:[0,0,0]
	v_mfma_scale_f32_16x16x128_f8f6f4 v[110:113], v[2:9], v[42:49], v[110:113], v248, v248 op_sel_hi:[0,0,0]
	v_mfma_scale_f32_16x16x128_f8f6f4 v[106:109], v[10:17], v[42:49], v[106:109], v248, v248 op_sel_hi:[0,0,0]
	v_mfma_scale_f32_16x16x128_f8f6f4 v[94:97], v[2:9], v[50:57], v[94:97], v248, v248 op_sel_hi:[0,0,0]
	v_mfma_scale_f32_16x16x128_f8f6f4 v[90:93], v[10:17], v[50:57], v[90:93], v248, v248 op_sel_hi:[0,0,0]
	v_mfma_scale_f32_16x16x128_f8f6f4 v[78:81], v[2:9], v[58:65], v[78:81], v248, v248 op_sel_hi:[0,0,0]
	v_mfma_scale_f32_16x16x128_f8f6f4 v[74:77], v[10:17], v[58:65], v[74:77], v248, v248 op_sel_hi:[0,0,0]
	s_setprio 0
	s_setprio 1
	v_mfma_scale_f32_16x16x128_f8f6f4 v[118:121], v[18:25], v[34:41], v[118:121], v248, v248 op_sel_hi:[0,0,0]
	v_mfma_scale_f32_16x16x128_f8f6f4 v[114:117], v[26:33], v[34:41], v[114:117], v248, v248 op_sel_hi:[0,0,0]
	v_mfma_scale_f32_16x16x128_f8f6f4 v[102:105], v[18:25], v[42:49], v[102:105], v248, v248 op_sel_hi:[0,0,0]
	v_mfma_scale_f32_16x16x128_f8f6f4 v[98:101], v[26:33], v[42:49], v[98:101], v248, v248 op_sel_hi:[0,0,0]
	v_mfma_scale_f32_16x16x128_f8f6f4 v[86:89], v[18:25], v[50:57], v[86:89], v248, v248 op_sel_hi:[0,0,0]
	v_mfma_scale_f32_16x16x128_f8f6f4 v[82:85], v[26:33], v[50:57], v[82:85], v248, v248 op_sel_hi:[0,0,0]
	v_mfma_scale_f32_16x16x128_f8f6f4 v[70:73], v[18:25], v[58:65], v[70:73], v248, v248 op_sel_hi:[0,0,0]
	v_mfma_scale_f32_16x16x128_f8f6f4 v[66:69], v[26:33], v[58:65], v[66:69], v248, v248 op_sel_hi:[0,0,0]
	s_setprio 0
	s_barrier
	s_add_u32 s24, s24, 0x100
	s_addc_u32 s25, s25, 0
	s_cmp_lt_i32 s68, s53
	s_cbranch_scc0 .LBB0_1022

; #define PG8_STAGEA(bufoff, h, ap, kb, go) do { if constexpr (GATHER) { PG8_STAGE(bufoff, (const char*)g.A + (kb), go[h]); } else { PG8_STAGE(bufoff, (ap) + (h) * hstep, voffA); } } while (0)
; #define PG8_WAIT_L(n) asm volatile("s_waitcnt lgkmcnt(" #n ")" ::: "memory")
; #define PG8_WAIT_V8R() do { if (relax) { if (GATHER && wid == 0 && has_next) asm volatile("s_waitcnt vmcnt(%0)" :: "n"(9 + Epi::NSTORES) : "memory"); else asm volatile("s_waitcnt vmcnt(%0)" :: "n"(8 + Epi::NSTORES) : "memory"); } else PG8_WAIT_V(8); } while (0)
; #define PG8_BAR __builtin_amdgcn_s_barrier()
; #define PG8_SCHED __builtin_amdgcn_sched_barrier(0)
; template <class Epi, class Sched, bool GATHER, bool FP8 = false>
; __device__ __forceinline__ void gemm_phase(LAS unsigned char* lds, LAS int* idx, const Gemm g, const Sched& S, const Epi& E) {
;     ...
;             const int relax = __builtin_amdgcn_readfirstlane(((t == 0) && (ui > 0)) ? 1 : 0);
;             PG8_LDB(B0, 0, 0); PG8_LDB(B1, 0, 1); PG8_SCHED; PG8_LDA(At, 0, 0); PG8_STAGEA(PG8_SA(1, 1), 1, a1, k1, gc);
;             PG8_WAIT_V8R(); PG8_WAIT_L(0); PG8_BAR; PG8_MMA(0, 0, At, B0); PG8_MMA(0, 1, At, B1); PG8_BAR; PG8_SCHED;
.LBB0_1020:
	s_andn2_b64 vcc, exec, s[30:31]
	s_cbranch_vccnz .LBB0_1013
	s_waitcnt vmcnt(24)
	s_branch .LBB0_1013
.Lpl1014_1014:
	ds_read_b128 v[26:29], v228
	ds_read_b128 v[30:33], v229
	ds_read_b128 v[18:21], v232
	ds_read_b128 v[22:25], v233
	ds_read_b128 v[10:13], v234
	ds_read_b128 v[14:17], v235
	ds_read_b128 v[2:5], v236
	ds_read_b128 v[6:9], v237
	s_cmp_eq_u32 s68, 0
	s_cselect_b64 s[26:27], -1, 0
	s_and_b64 s[26:27], s[8:9], s[26:27]
	v_lshl_add_u64 v[216:217], v[212:213], 0, s[24:25]
	s_add_i32 m0, s38, 0xc000
	ds_read_b128 v[58:61], v247
	ds_read_b128 v[62:65], v247 offset:1024
	ds_read_b128 v[50:53], v247 offset:2048
	ds_read_b128 v[54:57], v247 offset:3072
	ds_read_b128 v[42:45], v247 offset:4096
	ds_read_b128 v[46:49], v247 offset:5120
	ds_read_b128 v[34:37], v247 offset:6144
	ds_read_b128 v[38:41], v247 offset:7168
	global_load_lds_dwordx4 v[216:217], off
	v_lshl_add_u64 v[216:217], v[214:215], 0, s[24:25]
	s_add_i32 m0, s38, 0xe000
	s_nop 0
	global_load_lds_dwordx4 v[216:217], off
	s_and_b64 vcc, exec, s[26:27]
	s_not_b64 s[28:29], s[26:27]
	s_mov_b64 s[26:27], -1
	s_cbranch_vccnz .Lpl1014_1016
	s_waitcnt vmcnt(8)
	s_mov_b64 s[26:27], 0

; #define PG8_STAGE(bufoff, gbase, voff) do { _Pragma("unroll") for (int _i = 0; _i < 2; ++_i) \
;         __builtin_amdgcn_global_load_lds((const unsigned*)((const char*)(gbase) + (voff)[_i]), (LAS unsigned*)(lds + (bufoff) + ldsw + _i * 8192), 16, 0, 0); } while (0)
; #define PG8_STAGEA(bufoff, h, ap, kb, go) do { if constexpr (GATHER) { PG8_STAGE(bufoff, (const char*)g.A + (kb), go[h]); } else { PG8_STAGE(bufoff, (ap) + (h) * hstep, voffA); } } while (0)
; #define PG8_WAIT_L(n) asm volatile("s_waitcnt lgkmcnt(" #n ")" ::: "memory")
; #define PG8_WAIT_V8R() do { if (relax) { if (GATHER && wid == 0 && has_next) asm volatile("s_waitcnt vmcnt(%0)" :: "n"(9 + Epi::NSTORES) : "memory"); else asm volatile("s_waitcnt vmcnt(%0)" :: "n"(8 + Epi::NSTORES) : "memory"); } else PG8_WAIT_V(8); } while (0)
; #define PG8_BAR __builtin_amdgcn_s_barrier()
; template <class Epi, class Sched, bool GATHER, bool FP8 = false>
; __device__ __forceinline__ void gemm_phase(LAS unsigned char* lds, LAS int* idx, const Gemm g, const Sched& S, const Epi& E) {
;     ...
;             const bool last = (t == nt - 2);
;             const char* a1 = cA + (size_t)(t + 1) * kstep;
;             const char* a2 = last ? nA : cA + (size_t)(t + 2) * kstep; const char* b2 = last ? nB : cB + (size_t)(t + 2) * kstep;
;             const char* a3 = a2 + kstep; const char* b3 = b2 + kstep;
;             const size_t k1 = (size_t)(t + 1) * kstep, k2 = last ? (size_t)0 : (size_t)(t + 2) * kstep, k3 = k2 + kstep;
;             unsigned g2[2][2];
; #pragma unroll
;             for (int h = 0; h < 2; ++h)
; #pragma unroll
;                 for (int i = 0; i < 2; ++i) g2[h][i] = gc[h][i];
;             if constexpr (GATHER) { if (last && has_next) PG8_GIDX(g2, ((ui + 1) & 1) * BM); }
;             const int relax = __builtin_amdgcn_readfirstlane(((t == 0) && (ui > 0)) ? 1 : 0);
;             PG8_LDB(B0, 0, 0); PG8_LDB(B1, 0, 1); PG8_SCHED; PG8_LDA(At, 0, 0); PG8_STAGEA(PG8_SA(1, 1), 1, a1, k1, gc);
;             PG8_WAIT_V8R(); PG8_WAIT_L(0); PG8_BAR; PG8_MMA(0, 0, At, B0); PG8_MMA(0, 1, At, B1); PG8_BAR; PG8_SCHED;
;             PG8_LDA(At, 0, 1); PG8_STAGE(PG8_SB(0, 0), b2, voffB); PG8_STAGE(PG8_SB(0, 1), b2 + hstepB, voffB); PG8_STAGEA(PG8_SA(0, 0), 0, a2, k2, g2);
;             PG8_WAIT_V8R(); PG8_WAIT_L(0); PG8_BAR; PG8_MMA(1, 0, At, B0); PG8_MMA(1, 1, At, B1); PG8_BAR; PG8_SCHED;
.Lpl1014_1018:
	s_add_u32 s26, s22, s24
	s_addc_u32 s27, s23, s25
	s_add_u32 s26, s26, 0x100
	s_addc_u32 s27, s27, 0
	s_add_u32 s30, s69, s24
	s_addc_u32 s31, s70, s25
	s_waitcnt lgkmcnt(0)
	s_cmp_eq_u32 s55, s68
	s_cselect_b32 s27, s19, s27
	s_cselect_b32 s26, s18, s26
	s_cselect_b32 s31, s21, s31
	s_cselect_b32 s30, s20, s30
	s_barrier
	s_setprio 1
	s_waitcnt lgkmcnt(0)
	v_mfma_scale_f32_16x16x128_f8f6f4 v[190:193], v[26:33], v[58:65], 0, v248, v248 op_sel_hi:[0,0,0]
	v_mfma_scale_f32_16x16x128_f8f6f4 v[186:189], v[18:25], v[58:65], 0, v248, v248 op_sel_hi:[0,0,0]
	v_mfma_scale_f32_16x16x128_f8f6f4 v[174:177], v[26:33], v[50:57], 0, v248, v248 op_sel_hi:[0,0,0]
	v_mfma_scale_f32_16x16x128_f8f6f4 v[170:173], v[18:25], v[50:57], 0, v248, v248 op_sel_hi:[0,0,0]
	v_mfma_scale_f32_16x16x128_f8f6f4 v[158:161], v[26:33], v[42:49], 0, v248, v248 op_sel_hi:[0,0,0]
	v_mfma_scale_f32_16x16x128_f8f6f4 v[154:157], v[18:25], v[42:49], 0, v248, v248 op_sel_hi:[0,0,0]
	v_mfma_scale_f32_16x16x128_f8f6f4 v[142:145], v[26:33], v[34:41], 0, v248, v248 op_sel_hi:[0,0,0]
	v_mfma_scale_f32_16x16x128_f8f6f4 v[138:141], v[18:25], v[34:41], 0, v248, v248 op_sel_hi:[0,0,0]
	s_setprio 0
	s_setprio 1
	v_mfma_scale_f32_16x16x128_f8f6f4 v[182:185], v[10:17], v[58:65], 0, v248, v248 op_sel_hi:[0,0,0]
	v_mfma_scale_f32_16x16x128_f8f6f4 v[178:181], v[2:9], v[58:65], 0, v248, v248 op_sel_hi:[0,0,0]
	v_mfma_scale_f32_16x16x128_f8f6f4 v[166:169], v[10:17], v[50:57], 0, v248, v248 op_sel_hi:[0,0,0]
	v_mfma_scale_f32_16x16x128_f8f6f4 v[162:165], v[2:9], v[50:57], 0, v248, v248 op_sel_hi:[0,0,0]
	v_mfma_scale_f32_16x16x128_f8f6f4 v[150:153], v[10:17], v[42:49], 0, v248, v248 op_sel_hi:[0,0,0]
	v_mfma_scale_f32_16x16x128_f8f6f4 v[146:149], v[2:9], v[42:49], 0, v248, v248 op_sel_hi:[0,0,0]
	v_mfma_scale_f32_16x16x128_f8f6f4 v[134:137], v[10:17], v[34:41], 0, v248, v248 op_sel_hi:[0,0,0]
	v_mfma_scale_f32_16x16x128_f8f6f4 v[130:133], v[2:9], v[34:41], 0, v248, v248 op_sel_hi:[0,0,0]
	s_setprio 0
	s_barrier
	s_mov_b32 m0, s39
	v_lshl_add_u64 v[216:217], s[30:31], 0, v[196:197]
	v_lshl_add_u64 v[218:219], s[30:31], 0, v[200:201]
	s_add_u32 s30, s30, s10
	ds_read_b128 v[58:61], v247 offset:16384
	ds_read_b128 v[62:65], v247 offset:17408
	ds_read_b128 v[50:53], v247 offset:18432
	ds_read_b128 v[54:57], v247 offset:19456
	ds_read_b128 v[42:45], v247 offset:20480
	ds_read_b128 v[46:49], v247 offset:21504
	ds_read_b128 v[34:37], v247 offset:22528
	ds_read_b128 v[38:41], v247 offset:23552
	global_load_lds_dwordx4 v[216:217], off
	s_mov_b32 m0, s40
	s_addc_u32 s31, s31, s11
	global_load_lds_dwordx4 v[218:219], off
	v_lshl_add_u64 v[220:221], s[30:31], 0, v[196:197]
	s_mov_b32 m0, s41
	v_lshl_add_u64 v[222:223], s[30:31], 0, v[200:201]
	global_load_lds_dwordx4 v[220:221], off
	s_mov_b32 m0, s42
	v_lshl_add_u64 v[224:225], s[26:27], 0, v[194:195]
	global_load_lds_dwordx4 v[222:223], off
	s_mov_b32 m0, s38
	v_lshl_add_u64 v[226:227], s[26:27], 0, v[198:199]
	global_load_lds_dwordx4 v[224:225], off
	s_mov_b32 m0, s43
	s_mov_b64 s[30:31], -1
	global_load_lds_dwordx4 v[226:227], off
	s_and_b64 vcc, exec, s[28:29]
	s_cbranch_vccz .Lpl1014_1020
	s_waitcnt vmcnt(8)
	s_mov_b64 s[30:31], 0

; #define PG8_STAGE(bufoff, gbase, voff) do { _Pragma("unroll") for (int _i = 0; _i < 2; ++_i) \
;         __builtin_amdgcn_global_load_lds((const unsigned*)((const char*)(gbase) + (voff)[_i]), (LAS unsigned*)(lds + (bufoff) + ldsw + _i * 8192), 16, 0, 0); } while (0)
; #define PG8_STAGEA(bufoff, h, ap, kb, go) do { if constexpr (GATHER) { PG8_STAGE(bufoff, (const char*)g.A + (kb), go[h]); } else { PG8_STAGE(bufoff, (ap) + (h) * hstep, voffA); } } while (0)
; #define PG8_WAIT_V(n) asm volatile("s_waitcnt vmcnt(" #n ")" ::: "memory")
; #define PG8_WAIT_L(n) asm volatile("s_waitcnt lgkmcnt(" #n ")" ::: "memory")
; #define PG8_WAIT_V8R() do { if (relax) { if (GATHER && wid == 0 && has_next) asm volatile("s_waitcnt vmcnt(%0)" :: "n"(9 + Epi::NSTORES) : "memory"); else asm volatile("s_waitcnt vmcnt(%0)" :: "n"(8 + Epi::NSTORES) : "memory"); } else PG8_WAIT_V(8); } while (0)
; #define PG8_BAR __builtin_amdgcn_s_barrier()
; #define PG8_SCHED __builtin_amdgcn_sched_barrier(0)
; template <class Epi, class Sched, bool GATHER, bool FP8 = false>
; __device__ __forceinline__ void gemm_phase(LAS unsigned char* lds, LAS int* idx, const Gemm g, const Sched& S, const Epi& E) {
;     ...
;             PG8_WAIT_V8R(); PG8_WAIT_L(0); PG8_BAR; PG8_MMA(1, 0, At, B0); PG8_MMA(1, 1, At, B1); PG8_BAR; PG8_SCHED;
;             PG8_LDB(B0, 1, 0); PG8_LDB(B1, 1, 1); PG8_SCHED; PG8_LDA(At, 1, 0); PG8_STAGEA(PG8_SA(0, 1), 1, a2, k2, g2);
;             PG8_WAIT_V(8); PG8_WAIT_L(0); PG8_BAR; PG8_MMA(0, 0, At, B0); PG8_MMA(0, 1, At, B1); PG8_BAR; PG8_SCHED;
;             PG8_LDA(At, 1, 1); PG8_STAGE(PG8_SB(1, 0), b3, voffB); PG8_STAGE(PG8_SB(1, 1), b3 + hstepB, voffB); PG8_STAGEA(PG8_SA(1, 0), 0, a3, k3, g2);
;             PG8_WAIT_V(8); PG8_WAIT_L(0); PG8_BAR; PG8_MMA(1, 0, At, B0); PG8_MMA(1, 1, At, B1); PG8_BAR; PG8_SCHED;
;             if constexpr (GATHER) { if (last) { _Pragma("unroll") for (int h = 0; h < 2; ++h) _Pragma("unroll") for (int i = 0; i < 2; ++i) gc[h][i] = g2[h][i]; } }
;             t += 2;
.Lpl1014_1013:
	s_waitcnt lgkmcnt(0)
	s_add_i32 s68, s68, 2
	s_barrier
	s_setprio 1
	s_waitcnt lgkmcnt(0)
	v_mfma_scale_f32_16x16x128_f8f6f4 v[126:129], v[26:33], v[58:65], 0, v248, v248 op_sel_hi:[0,0,0]
	v_mfma_scale_f32_16x16x128_f8f6f4 v[122:125], v[18:25], v[58:65], 0, v248, v248 op_sel_hi:[0,0,0]
	v_mfma_scale_f32_16x16x128_f8f6f4 v[110:113], v[26:33], v[50:57], 0, v248, v248 op_sel_hi:[0,0,0]
	v_mfma_scale_f32_16x16x128_f8f6f4 v[106:109], v[18:25], v[50:57], 0, v248, v248 op_sel_hi:[0,0,0]
	v_mfma_scale_f32_16x16x128_f8f6f4 v[94:97], v[26:33], v[42:49], 0, v248, v248 op_sel_hi:[0,0,0]
	v_mfma_scale_f32_16x16x128_f8f6f4 v[90:93], v[18:25], v[42:49], 0, v248, v248 op_sel_hi:[0,0,0]
	v_mfma_scale_f32_16x16x128_f8f6f4 v[78:81], v[26:33], v[34:41], 0, v248, v248 op_sel_hi:[0,0,0]
	v_mfma_scale_f32_16x16x128_f8f6f4 v[74:77], v[18:25], v[34:41], 0, v248, v248 op_sel_hi:[0,0,0]
	s_setprio 0
	s_setprio 1
	v_mfma_scale_f32_16x16x128_f8f6f4 v[118:121], v[10:17], v[58:65], 0, v248, v248 op_sel_hi:[0,0,0]
	v_mfma_scale_f32_16x16x128_f8f6f4 v[114:117], v[2:9], v[58:65], 0, v248, v248 op_sel_hi:[0,0,0]
	v_mfma_scale_f32_16x16x128_f8f6f4 v[102:105], v[10:17], v[50:57], 0, v248, v248 op_sel_hi:[0,0,0]
	v_mfma_scale_f32_16x16x128_f8f6f4 v[98:101], v[2:9], v[50:57], 0, v248, v248 op_sel_hi:[0,0,0]
	v_mfma_scale_f32_16x16x128_f8f6f4 v[86:89], v[10:17], v[42:49], 0, v248, v248 op_sel_hi:[0,0,0]
	v_mfma_scale_f32_16x16x128_f8f6f4 v[82:85], v[2:9], v[42:49], 0, v248, v248 op_sel_hi:[0,0,0]
	v_mfma_scale_f32_16x16x128_f8f6f4 v[70:73], v[10:17], v[34:41], 0, v248, v248 op_sel_hi:[0,0,0]
	v_mfma_scale_f32_16x16x128_f8f6f4 v[66:69], v[2:9], v[34:41], 0, v248, v248 op_sel_hi:[0,0,0]
	s_branch .Lpl1014_join
